# adds: GU epilogue SiLU*up*weight math issued as packed f32 pairs (same operations, identical results)
# speedup vs baseline: 1.0050x; 1.0050x over previous
; __device__ __forceinline__ unsigned pk4f8(float a, float b, float c, float d) { int w = 0; w = __builtin_amdgcn_cvt_pk_fp8_f32(a, b, w, false); w = __builtin_amdgcn_cvt_pk_fp8_f32(c, d, w, true); return (unsigned)w; }
;     __device__ __forceinline__ void operator()(const f32x4 (&acc)[2][2][4][2], const Unit& u, int wr, int wc, int fr, int fq) const {
;     ...
;                 for (int dm = 0; dm < 2; ++dm) { const int m = mp + dm; const int row = row0 + ai * HALF + m * 16; const float w = swt[row];
;                     float h[8];
; #pragma unroll
;                     for (int n = 0; n < 2; ++n)
; #pragma unroll
;                         for (int j = 0; j < 4; ++j) { const float g = acc[ai][0][m][n][j], up = acc[ai][1][m][n][j];
;                             const float s = g * __builtin_amdgcn_rcpf(1.0f + __builtin_amdgcn_exp2f(-1.4426950408889634f * g)); h[n * 4 + j] = s * up * w; }
;                     pk[dm][0] = pk4f8(h[0], h[1], h[2], h[3]); pk[dm][1] = pk4f8(h[4], h[5], h[6], h[7]); }
.LBB0_1608:
	v_mov_b32_e32 v26, 0xbfb8aa3b
	s_lshl_b32 s0, s29, 8
	v_mov_b32_e32 v10, v200
	v_add_u32_e32 v0, s0, v165
	s_lshl_b32 s0, s44, 7
	v_and_or_b32 v8, v10, 15, v0
	v_ashrrev_i32_e32 v0, 1, v10
	v_ashrrev_i32_e32 v9, 31, v8
	s_or_b32 s0, s0, s6
	v_and_b32_e32 v0, -16, v0
	v_lshl_add_u64 v[6:7], v[8:9], 2, s[42:43]
	v_add_u32_e32 v4, s0, v0
	global_load_dword v18, v[6:7], off
	global_load_dword v19, v[6:7], off offset:64
	global_load_dword v20, v[6:7], off offset:128
	global_load_dword v21, v[6:7], off offset:192
	global_load_dword v22, v[6:7], off offset:512
	global_load_dword v23, v[6:7], off offset:576
	global_load_dword v24, v[6:7], off offset:640
	global_load_dword v25, v[6:7], off offset:704
	v_ashrrev_i32_e32 v5, 31, v4
	s_mov_b64 s[0:1], -1
	s_and_b64 vcc, exec, s[38:39]
	v_mov_b32_e32 v242, v218
	v_mov_b32_e32 v243, v214
	v_mov_b32_e32 v244, v201
	v_pk_mul_f32 v[192:193], v[152:153], v[26:27] op_sel_hi:[1,0]
	v_pk_mul_f32 v[194:195], v[154:155], v[26:27] op_sel_hi:[1,0]
	v_pk_mul_f32 v[196:197], v[156:157], v[26:27] op_sel_hi:[1,0]
	v_pk_mul_f32 v[198:199], v[158:159], v[26:27] op_sel_hi:[1,0]
	v_exp_f32_e32 v192, v192
	v_exp_f32_e32 v193, v193
	v_exp_f32_e32 v194, v194
	v_exp_f32_e32 v195, v195
	v_exp_f32_e32 v196, v196
	v_exp_f32_e32 v197, v197
	v_exp_f32_e32 v198, v198
	v_exp_f32_e32 v199, v199
	v_pk_add_f32 v[192:193], v[192:193], 1.0 op_sel_hi:[1,0]
	v_pk_add_f32 v[194:195], v[194:195], 1.0 op_sel_hi:[1,0]
	v_pk_add_f32 v[196:197], v[196:197], 1.0 op_sel_hi:[1,0]
	v_pk_add_f32 v[198:199], v[198:199], 1.0 op_sel_hi:[1,0]
	v_rcp_f32_e32 v192, v192
	v_rcp_f32_e32 v193, v193
	v_rcp_f32_e32 v194, v194
	v_rcp_f32_e32 v195, v195
	v_rcp_f32_e32 v196, v196
	v_rcp_f32_e32 v197, v197
	v_rcp_f32_e32 v198, v198
	v_rcp_f32_e32 v199, v199
	v_pk_mul_f32 v[192:193], v[152:153], v[192:193]
	v_pk_mul_f32 v[194:195], v[154:155], v[194:195]
	v_pk_mul_f32 v[196:197], v[156:157], v[196:197]
	v_pk_mul_f32 v[198:199], v[158:159], v[198:199]
	v_pk_mul_f32 v[192:193], v[192:193], v[144:145]
	v_pk_mul_f32 v[194:195], v[194:195], v[146:147]
	v_pk_mul_f32 v[196:197], v[196:197], v[148:149]
	v_pk_mul_f32 v[198:199], v[198:199], v[150:151]
	s_waitcnt vmcnt(7)
	v_pk_mul_f32 v[192:193], v[192:193], v[18:19] op_sel_hi:[1,0]
	v_pk_mul_f32 v[194:195], v[194:195], v[18:19] op_sel_hi:[1,0]
	v_pk_mul_f32 v[196:197], v[196:197], v[18:19] op_sel_hi:[1,0]
	v_pk_mul_f32 v[198:199], v[198:199], v[18:19] op_sel_hi:[1,0]
	v_mov_b32_e32 v0, v181
	v_cvt_pk_fp8_f32 v0, v196, v197
	v_mov_b32_e32 v1, v181
	v_cvt_pk_fp8_f32 v1, v192, v193
	v_cvt_pk_fp8_f32 v0, v198, v199 op_sel:[0,0,1]
	v_cvt_pk_fp8_f32 v1, v194, v195 op_sel:[0,0,1]
	v_pk_mul_f32 v[202:203], v[132:133], v[26:27] op_sel_hi:[1,0]
	v_pk_mul_f32 v[204:205], v[134:135], v[26:27] op_sel_hi:[1,0]
	v_pk_mul_f32 v[206:207], v[140:141], v[26:27] op_sel_hi:[1,0]
	v_pk_mul_f32 v[208:209], v[142:143], v[26:27] op_sel_hi:[1,0]
	v_exp_f32_e32 v202, v202
	v_exp_f32_e32 v203, v203
	v_exp_f32_e32 v204, v204
	v_exp_f32_e32 v205, v205
	v_exp_f32_e32 v206, v206
	v_exp_f32_e32 v207, v207
	v_exp_f32_e32 v208, v208
	v_exp_f32_e32 v209, v209
	v_pk_add_f32 v[202:203], v[202:203], 1.0 op_sel_hi:[1,0]
	v_pk_add_f32 v[204:205], v[204:205], 1.0 op_sel_hi:[1,0]
	v_pk_add_f32 v[206:207], v[206:207], 1.0 op_sel_hi:[1,0]
	v_pk_add_f32 v[208:209], v[208:209], 1.0 op_sel_hi:[1,0]
	v_rcp_f32_e32 v202, v202
	v_rcp_f32_e32 v203, v203
	v_rcp_f32_e32 v204, v204
	v_rcp_f32_e32 v205, v205
	v_rcp_f32_e32 v206, v206
	v_rcp_f32_e32 v207, v207
	v_rcp_f32_e32 v208, v208
	v_rcp_f32_e32 v209, v209
	v_pk_mul_f32 v[202:203], v[132:133], v[202:203]
	v_pk_mul_f32 v[204:205], v[134:135], v[204:205]
	v_pk_mul_f32 v[206:207], v[140:141], v[206:207]
	v_pk_mul_f32 v[208:209], v[142:143], v[208:209]
	v_pk_mul_f32 v[202:203], v[202:203], v[128:129]
	v_pk_mul_f32 v[204:205], v[204:205], v[130:131]
	v_pk_mul_f32 v[206:207], v[206:207], v[136:137]
	v_pk_mul_f32 v[208:209], v[208:209], v[138:139]
	s_waitcnt vmcnt(6)
	v_pk_mul_f32 v[202:203], v[202:203], v[18:19] op_sel:[0,1] op_sel_hi:[1,1]
	v_pk_mul_f32 v[204:205], v[204:205], v[18:19] op_sel:[0,1] op_sel_hi:[1,1]
	v_pk_mul_f32 v[206:207], v[206:207], v[18:19] op_sel:[0,1] op_sel_hi:[1,1]
	v_pk_mul_f32 v[208:209], v[208:209], v[18:19] op_sel:[0,1] op_sel_hi:[1,1]
	v_mov_b32_e32 v2, v181
	v_cvt_pk_fp8_f32 v2, v206, v207
	v_mov_b32_e32 v3, v181
	v_cvt_pk_fp8_f32 v3, v202, v203
	v_and_b32_e32 v9, 16, v10
	v_cvt_pk_fp8_f32 v2, v208, v209 op_sel:[0,0,1]
	v_or_b32_e32 v10, v8, v9
	v_cvt_pk_fp8_f32 v3, v204, v205 op_sel:[0,0,1]
	v_ashrrev_i32_e32 v11, 31, v10
	v_lshlrev_b64 v[10:11], 8, v[10:11]
	v_lshl_add_u64 v[10:11], s[40:41], 0, v[10:11]
	v_permlane16_swap_b32_e32 v0, v2
	v_permlane16_swap_b32_e32 v1, v3
	v_lshl_add_u64 v[10:11], v[10:11], 0, v[4:5]
	global_store_dwordx4 v[10:11], v[0:3], off
	s_nop 1
	v_pk_mul_f32 v[192:193], v[120:121], v[26:27] op_sel_hi:[1,0]
	v_pk_mul_f32 v[194:195], v[122:123], v[26:27] op_sel_hi:[1,0]
	v_pk_mul_f32 v[196:197], v[124:125], v[26:27] op_sel_hi:[1,0]
	v_pk_mul_f32 v[198:199], v[126:127], v[26:27] op_sel_hi:[1,0]
	v_exp_f32_e32 v192, v192
	v_exp_f32_e32 v193, v193
	v_exp_f32_e32 v194, v194
	v_exp_f32_e32 v195, v195
	v_exp_f32_e32 v196, v196
	v_exp_f32_e32 v197, v197
	v_exp_f32_e32 v198, v198
	v_exp_f32_e32 v199, v199
	v_pk_add_f32 v[192:193], v[192:193], 1.0 op_sel_hi:[1,0]
	v_pk_add_f32 v[194:195], v[194:195], 1.0 op_sel_hi:[1,0]
	v_pk_add_f32 v[196:197], v[196:197], 1.0 op_sel_hi:[1,0]
	v_pk_add_f32 v[198:199], v[198:199], 1.0 op_sel_hi:[1,0]
	v_rcp_f32_e32 v192, v192
	v_rcp_f32_e32 v193, v193
	v_rcp_f32_e32 v194, v194
	v_rcp_f32_e32 v195, v195
	v_rcp_f32_e32 v196, v196
	v_rcp_f32_e32 v197, v197
	v_rcp_f32_e32 v198, v198
	v_rcp_f32_e32 v199, v199
	v_pk_mul_f32 v[192:193], v[120:121], v[192:193]
	v_pk_mul_f32 v[194:195], v[122:123], v[194:195]
	v_pk_mul_f32 v[196:197], v[124:125], v[196:197]
	v_pk_mul_f32 v[198:199], v[126:127], v[198:199]
	v_pk_mul_f32 v[192:193], v[192:193], v[112:113]
	v_pk_mul_f32 v[194:195], v[194:195], v[114:115]
	v_pk_mul_f32 v[196:197], v[196:197], v[116:117]
	v_pk_mul_f32 v[198:199], v[198:199], v[118:119]
	s_waitcnt vmcnt(6)
; __device__ __forceinline__ unsigned pk4f8(float a, float b, float c, float d) { int w = 0; w = __builtin_amdgcn_cvt_pk_fp8_f32(a, b, w, false); w = __builtin_amdgcn_cvt_pk_fp8_f32(c, d, w, true); return (unsigned)w; }
;     __device__ __forceinline__ void operator()(const f32x4 (&acc)[2][2][4][2], const Unit& u, int wr, int wc, int fr, int fq) const {
;     ...
;                 for (int dm = 0; dm < 2; ++dm) { const int m = mp + dm; const int row = row0 + ai * HALF + m * 16; const float w = swt[row];
;                     float h[8];
; #pragma unroll
;                     for (int n = 0; n < 2; ++n)
; #pragma unroll
;                         for (int j = 0; j < 4; ++j) { const float g = acc[ai][0][m][n][j], up = acc[ai][1][m][n][j];
;                             const float s = g * __builtin_amdgcn_rcpf(1.0f + __builtin_amdgcn_exp2f(-1.4426950408889634f * g)); h[n * 4 + j] = s * up * w; }
;                     pk[dm][0] = pk4f8(h[0], h[1], h[2], h[3]); pk[dm][1] = pk4f8(h[4], h[5], h[6], h[7]); }
	v_pk_mul_f32 v[192:193], v[192:193], v[20:21] op_sel_hi:[1,0]
	v_pk_mul_f32 v[194:195], v[194:195], v[20:21] op_sel_hi:[1,0]
	v_pk_mul_f32 v[196:197], v[196:197], v[20:21] op_sel_hi:[1,0]
	v_pk_mul_f32 v[198:199], v[198:199], v[20:21] op_sel_hi:[1,0]
	v_mov_b32_e32 v0, v181
	v_cvt_pk_fp8_f32 v0, v196, v197
	v_mov_b32_e32 v1, v181
	v_cvt_pk_fp8_f32 v1, v192, v193
	v_cvt_pk_fp8_f32 v0, v198, v199 op_sel:[0,0,1]
	v_cvt_pk_fp8_f32 v1, v194, v195 op_sel:[0,0,1]
	v_pk_mul_f32 v[202:203], v[100:101], v[26:27] op_sel_hi:[1,0]
	v_pk_mul_f32 v[204:205], v[102:103], v[26:27] op_sel_hi:[1,0]
	v_pk_mul_f32 v[206:207], v[108:109], v[26:27] op_sel_hi:[1,0]
	v_pk_mul_f32 v[208:209], v[110:111], v[26:27] op_sel_hi:[1,0]
	v_exp_f32_e32 v202, v202
	v_exp_f32_e32 v203, v203
	v_exp_f32_e32 v204, v204
	v_exp_f32_e32 v205, v205
	v_exp_f32_e32 v206, v206
	v_exp_f32_e32 v207, v207
	v_exp_f32_e32 v208, v208
	v_exp_f32_e32 v209, v209
	v_pk_add_f32 v[202:203], v[202:203], 1.0 op_sel_hi:[1,0]
	v_pk_add_f32 v[204:205], v[204:205], 1.0 op_sel_hi:[1,0]
	v_pk_add_f32 v[206:207], v[206:207], 1.0 op_sel_hi:[1,0]
	v_pk_add_f32 v[208:209], v[208:209], 1.0 op_sel_hi:[1,0]
	v_rcp_f32_e32 v202, v202
	v_rcp_f32_e32 v203, v203
	v_rcp_f32_e32 v204, v204
	v_rcp_f32_e32 v205, v205
	v_rcp_f32_e32 v206, v206
	v_rcp_f32_e32 v207, v207
	v_rcp_f32_e32 v208, v208
	v_rcp_f32_e32 v209, v209
	v_pk_mul_f32 v[202:203], v[100:101], v[202:203]
	v_pk_mul_f32 v[204:205], v[102:103], v[204:205]
	v_pk_mul_f32 v[206:207], v[108:109], v[206:207]
	v_pk_mul_f32 v[208:209], v[110:111], v[208:209]
	v_pk_mul_f32 v[202:203], v[202:203], v[96:97]
	v_pk_mul_f32 v[204:205], v[204:205], v[98:99]
	v_pk_mul_f32 v[206:207], v[206:207], v[104:105]
	v_pk_mul_f32 v[208:209], v[208:209], v[106:107]
	s_waitcnt vmcnt(5)
	v_pk_mul_f32 v[202:203], v[202:203], v[20:21] op_sel:[0,1] op_sel_hi:[1,1]
	v_pk_mul_f32 v[204:205], v[204:205], v[20:21] op_sel:[0,1] op_sel_hi:[1,1]
	v_pk_mul_f32 v[206:207], v[206:207], v[20:21] op_sel:[0,1] op_sel_hi:[1,1]
	v_pk_mul_f32 v[208:209], v[208:209], v[20:21] op_sel:[0,1] op_sel_hi:[1,1]
	v_mov_b32_e32 v2, v181
	v_cvt_pk_fp8_f32 v2, v206, v207
	v_mov_b32_e32 v3, v181
	v_cvt_pk_fp8_f32 v3, v202, v203
	v_or_b32_e32 v10, 32, v9
	v_cvt_pk_fp8_f32 v2, v208, v209 op_sel:[0,0,1]
	v_or_b32_e32 v12, v10, v8
	v_cvt_pk_fp8_f32 v3, v204, v205 op_sel:[0,0,1]
	v_ashrrev_i32_e32 v13, 31, v12
	v_lshlrev_b64 v[12:13], 8, v[12:13]
	v_lshl_add_u64 v[12:13], s[40:41], 0, v[12:13]
	v_permlane16_swap_b32_e32 v0, v2
	v_permlane16_swap_b32_e32 v1, v3
	v_lshl_add_u64 v[12:13], v[12:13], 0, v[4:5]
	global_store_dwordx4 v[12:13], v[0:3], off
	s_nop 1
	v_add_u32_e32 v8, 0x80, v8
	v_pk_mul_f32 v[192:193], v[88:89], v[26:27] op_sel_hi:[1,0]
	v_pk_mul_f32 v[194:195], v[90:91], v[26:27] op_sel_hi:[1,0]
	v_pk_mul_f32 v[196:197], v[92:93], v[26:27] op_sel_hi:[1,0]
	v_pk_mul_f32 v[198:199], v[94:95], v[26:27] op_sel_hi:[1,0]
	v_exp_f32_e32 v192, v192
	v_exp_f32_e32 v193, v193
	v_exp_f32_e32 v194, v194
	v_exp_f32_e32 v195, v195
	v_exp_f32_e32 v196, v196
	v_exp_f32_e32 v197, v197
	v_exp_f32_e32 v198, v198
	v_exp_f32_e32 v199, v199
	v_pk_add_f32 v[192:193], v[192:193], 1.0 op_sel_hi:[1,0]
	v_pk_add_f32 v[194:195], v[194:195], 1.0 op_sel_hi:[1,0]
	v_pk_add_f32 v[196:197], v[196:197], 1.0 op_sel_hi:[1,0]
	v_pk_add_f32 v[198:199], v[198:199], 1.0 op_sel_hi:[1,0]
	v_rcp_f32_e32 v192, v192
	v_rcp_f32_e32 v193, v193
	v_rcp_f32_e32 v194, v194
	v_rcp_f32_e32 v195, v195
	v_rcp_f32_e32 v196, v196
	v_rcp_f32_e32 v197, v197
	v_rcp_f32_e32 v198, v198
	v_rcp_f32_e32 v199, v199
	v_pk_mul_f32 v[192:193], v[88:89], v[192:193]
	v_pk_mul_f32 v[194:195], v[90:91], v[194:195]
	v_pk_mul_f32 v[196:197], v[92:93], v[196:197]
	v_pk_mul_f32 v[198:199], v[94:95], v[198:199]
	v_pk_mul_f32 v[192:193], v[192:193], v[80:81]
	v_pk_mul_f32 v[194:195], v[194:195], v[82:83]
	v_pk_mul_f32 v[196:197], v[196:197], v[84:85]
	v_pk_mul_f32 v[198:199], v[198:199], v[86:87]
	s_waitcnt vmcnt(5)
	v_pk_mul_f32 v[192:193], v[192:193], v[22:23] op_sel_hi:[1,0]
	v_pk_mul_f32 v[194:195], v[194:195], v[22:23] op_sel_hi:[1,0]
	v_pk_mul_f32 v[196:197], v[196:197], v[22:23] op_sel_hi:[1,0]
	v_pk_mul_f32 v[198:199], v[198:199], v[22:23] op_sel_hi:[1,0]
	v_mov_b32_e32 v0, v181
	v_cvt_pk_fp8_f32 v0, v196, v197
	v_mov_b32_e32 v1, v181
	v_cvt_pk_fp8_f32 v1, v192, v193
	v_cvt_pk_fp8_f32 v0, v198, v199 op_sel:[0,0,1]
	v_cvt_pk_fp8_f32 v1, v194, v195 op_sel:[0,0,1]
	v_pk_mul_f32 v[202:203], v[68:69], v[26:27] op_sel_hi:[1,0]
	v_pk_mul_f32 v[204:205], v[70:71], v[26:27] op_sel_hi:[1,0]
	v_pk_mul_f32 v[206:207], v[76:77], v[26:27] op_sel_hi:[1,0]
	v_pk_mul_f32 v[208:209], v[78:79], v[26:27] op_sel_hi:[1,0]
	v_exp_f32_e32 v202, v202
	v_exp_f32_e32 v203, v203
	v_exp_f32_e32 v204, v204
	v_exp_f32_e32 v205, v205
	v_exp_f32_e32 v206, v206
	v_exp_f32_e32 v207, v207
	v_exp_f32_e32 v208, v208
	v_exp_f32_e32 v209, v209
	v_pk_add_f32 v[202:203], v[202:203], 1.0 op_sel_hi:[1,0]
	v_pk_add_f32 v[204:205], v[204:205], 1.0 op_sel_hi:[1,0]
	v_pk_add_f32 v[206:207], v[206:207], 1.0 op_sel_hi:[1,0]
	v_pk_add_f32 v[208:209], v[208:209], 1.0 op_sel_hi:[1,0]
	v_rcp_f32_e32 v202, v202
	v_rcp_f32_e32 v203, v203
	v_rcp_f32_e32 v204, v204
	v_rcp_f32_e32 v205, v205
	v_rcp_f32_e32 v206, v206
	v_rcp_f32_e32 v207, v207
	v_rcp_f32_e32 v208, v208
	v_rcp_f32_e32 v209, v209
	v_pk_mul_f32 v[202:203], v[68:69], v[202:203]
	v_pk_mul_f32 v[204:205], v[70:71], v[204:205]
	v_pk_mul_f32 v[206:207], v[76:77], v[206:207]
	v_pk_mul_f32 v[208:209], v[78:79], v[208:209]
	v_pk_mul_f32 v[202:203], v[202:203], v[64:65]
	v_pk_mul_f32 v[204:205], v[204:205], v[66:67]
	v_pk_mul_f32 v[206:207], v[206:207], v[72:73]
	v_pk_mul_f32 v[208:209], v[208:209], v[74:75]
	s_waitcnt vmcnt(4)
; __device__ __forceinline__ unsigned pk4f8(float a, float b, float c, float d) { int w = 0; w = __builtin_amdgcn_cvt_pk_fp8_f32(a, b, w, false); w = __builtin_amdgcn_cvt_pk_fp8_f32(c, d, w, true); return (unsigned)w; }
;     __device__ __forceinline__ void operator()(const f32x4 (&acc)[2][2][4][2], const Unit& u, int wr, int wc, int fr, int fq) const {
;     ...
;                 for (int dm = 0; dm < 2; ++dm) { const int m = mp + dm; const int row = row0 + ai * HALF + m * 16; const float w = swt[row];
;                     float h[8];
; #pragma unroll
;                     for (int n = 0; n < 2; ++n)
; #pragma unroll
;                         for (int j = 0; j < 4; ++j) { const float g = acc[ai][0][m][n][j], up = acc[ai][1][m][n][j];
;                             const float s = g * __builtin_amdgcn_rcpf(1.0f + __builtin_amdgcn_exp2f(-1.4426950408889634f * g)); h[n * 4 + j] = s * up * w; }
;                     pk[dm][0] = pk4f8(h[0], h[1], h[2], h[3]); pk[dm][1] = pk4f8(h[4], h[5], h[6], h[7]); }
;                 { auto r = __builtin_amdgcn_permlane16_swap(pk[0][0], pk[1][0], false, false); pk[0][0] = r[0]; pk[1][0] = r[1]; }
;                 { auto r = __builtin_amdgcn_permlane16_swap(pk[0][1], pk[1][1], false, false); pk[0][1] = r[0]; pk[1][1] = r[1]; }
;                 u32x4 o; o.x = pk[0][0]; o.y = pk[0][1]; o.z = pk[1][0]; o.w = pk[1][1];
;                 const int row = row0 + ai * HALF + (mp + (fq & 1)) * 16;
;                 *(u32x4*)(H + (size_t)row * 256 + col0) = o; }
	v_pk_mul_f32 v[202:203], v[202:203], v[22:23] op_sel:[0,1] op_sel_hi:[1,1]
	v_pk_mul_f32 v[204:205], v[204:205], v[22:23] op_sel:[0,1] op_sel_hi:[1,1]
	v_pk_mul_f32 v[206:207], v[206:207], v[22:23] op_sel:[0,1] op_sel_hi:[1,1]
	v_pk_mul_f32 v[208:209], v[208:209], v[22:23] op_sel:[0,1] op_sel_hi:[1,1]
	v_mov_b32_e32 v2, v181
	v_cvt_pk_fp8_f32 v2, v206, v207
	v_mov_b32_e32 v3, v181
	v_cvt_pk_fp8_f32 v3, v202, v203
	v_cvt_pk_fp8_f32 v2, v208, v209 op_sel:[0,0,1]
	v_or_b32_e32 v12, v8, v9
	v_cvt_pk_fp8_f32 v3, v204, v205 op_sel:[0,0,1]
	v_ashrrev_i32_e32 v13, 31, v12
	v_lshlrev_b64 v[12:13], 8, v[12:13]
	v_lshl_add_u64 v[12:13], s[40:41], 0, v[12:13]
	v_permlane16_swap_b32_e32 v0, v2
	v_permlane16_swap_b32_e32 v1, v3
	v_lshl_add_u64 v[12:13], v[12:13], 0, v[4:5]
	global_store_dwordx4 v[12:13], v[0:3], off
	s_nop 1
	v_pk_mul_f32 v[192:193], v[56:57], v[26:27] op_sel_hi:[1,0]
	v_pk_mul_f32 v[194:195], v[58:59], v[26:27] op_sel_hi:[1,0]
	v_pk_mul_f32 v[196:197], v[60:61], v[26:27] op_sel_hi:[1,0]
	v_pk_mul_f32 v[198:199], v[62:63], v[26:27] op_sel_hi:[1,0]
	v_exp_f32_e32 v192, v192
	v_exp_f32_e32 v193, v193
	v_exp_f32_e32 v194, v194
	v_exp_f32_e32 v195, v195
	v_exp_f32_e32 v196, v196
	v_exp_f32_e32 v197, v197
	v_exp_f32_e32 v198, v198
	v_exp_f32_e32 v199, v199
	v_pk_add_f32 v[192:193], v[192:193], 1.0 op_sel_hi:[1,0]
	v_pk_add_f32 v[194:195], v[194:195], 1.0 op_sel_hi:[1,0]
	v_pk_add_f32 v[196:197], v[196:197], 1.0 op_sel_hi:[1,0]
	v_pk_add_f32 v[198:199], v[198:199], 1.0 op_sel_hi:[1,0]
	v_rcp_f32_e32 v192, v192
	v_rcp_f32_e32 v193, v193
	v_rcp_f32_e32 v194, v194
	v_rcp_f32_e32 v195, v195
	v_rcp_f32_e32 v196, v196
	v_rcp_f32_e32 v197, v197
	v_rcp_f32_e32 v198, v198
	v_rcp_f32_e32 v199, v199
	v_pk_mul_f32 v[192:193], v[56:57], v[192:193]
	v_pk_mul_f32 v[194:195], v[58:59], v[194:195]
	v_pk_mul_f32 v[196:197], v[60:61], v[196:197]
	v_pk_mul_f32 v[198:199], v[62:63], v[198:199]
	v_pk_mul_f32 v[192:193], v[192:193], v[48:49]
	v_pk_mul_f32 v[194:195], v[194:195], v[50:51]
	v_pk_mul_f32 v[196:197], v[196:197], v[52:53]
	v_pk_mul_f32 v[198:199], v[198:199], v[54:55]
	s_waitcnt vmcnt(4)
	v_pk_mul_f32 v[192:193], v[192:193], v[24:25] op_sel_hi:[1,0]
	v_pk_mul_f32 v[194:195], v[194:195], v[24:25] op_sel_hi:[1,0]
	v_pk_mul_f32 v[196:197], v[196:197], v[24:25] op_sel_hi:[1,0]
	v_pk_mul_f32 v[198:199], v[198:199], v[24:25] op_sel_hi:[1,0]
	v_mov_b32_e32 v0, v181
	v_cvt_pk_fp8_f32 v0, v196, v197
	v_mov_b32_e32 v1, v181
	v_cvt_pk_fp8_f32 v1, v192, v193
	v_cvt_pk_fp8_f32 v0, v198, v199 op_sel:[0,0,1]
	v_cvt_pk_fp8_f32 v1, v194, v195 op_sel:[0,0,1]
	v_pk_mul_f32 v[202:203], v[36:37], v[26:27] op_sel_hi:[1,0]
	v_pk_mul_f32 v[204:205], v[38:39], v[26:27] op_sel_hi:[1,0]
	v_pk_mul_f32 v[206:207], v[44:45], v[26:27] op_sel_hi:[1,0]
	v_pk_mul_f32 v[208:209], v[46:47], v[26:27] op_sel_hi:[1,0]
	v_exp_f32_e32 v202, v202
	v_exp_f32_e32 v203, v203
	v_exp_f32_e32 v204, v204
	v_exp_f32_e32 v205, v205
	v_exp_f32_e32 v206, v206
	v_exp_f32_e32 v207, v207
	v_exp_f32_e32 v208, v208
	v_exp_f32_e32 v209, v209
	v_pk_add_f32 v[202:203], v[202:203], 1.0 op_sel_hi:[1,0]
	v_pk_add_f32 v[204:205], v[204:205], 1.0 op_sel_hi:[1,0]
	v_pk_add_f32 v[206:207], v[206:207], 1.0 op_sel_hi:[1,0]
	v_pk_add_f32 v[208:209], v[208:209], 1.0 op_sel_hi:[1,0]
	v_rcp_f32_e32 v202, v202
	v_rcp_f32_e32 v203, v203
	v_rcp_f32_e32 v204, v204
	v_rcp_f32_e32 v205, v205
	v_rcp_f32_e32 v206, v206
	v_rcp_f32_e32 v207, v207
	v_rcp_f32_e32 v208, v208
	v_rcp_f32_e32 v209, v209
	v_pk_mul_f32 v[202:203], v[36:37], v[202:203]
	v_pk_mul_f32 v[204:205], v[38:39], v[204:205]
	v_pk_mul_f32 v[206:207], v[44:45], v[206:207]
	v_pk_mul_f32 v[208:209], v[46:47], v[208:209]
	v_pk_mul_f32 v[202:203], v[202:203], v[32:33]
	v_pk_mul_f32 v[204:205], v[204:205], v[34:35]
	v_pk_mul_f32 v[206:207], v[206:207], v[40:41]
	v_pk_mul_f32 v[208:209], v[208:209], v[42:43]
	s_waitcnt vmcnt(3)
	v_pk_mul_f32 v[202:203], v[202:203], v[24:25] op_sel:[0,1] op_sel_hi:[1,1]
	v_pk_mul_f32 v[204:205], v[204:205], v[24:25] op_sel:[0,1] op_sel_hi:[1,1]
	v_pk_mul_f32 v[206:207], v[206:207], v[24:25] op_sel:[0,1] op_sel_hi:[1,1]
	v_pk_mul_f32 v[208:209], v[208:209], v[24:25] op_sel:[0,1] op_sel_hi:[1,1]
	v_mov_b32_e32 v2, v181
	v_cvt_pk_fp8_f32 v2, v206, v207
	v_mov_b32_e32 v3, v181
	v_cvt_pk_fp8_f32 v3, v202, v203
	v_or_b32_e32 v6, v8, v10
	v_cvt_pk_fp8_f32 v2, v208, v209 op_sel:[0,0,1]
	v_ashrrev_i32_e32 v7, 31, v6
	v_cvt_pk_fp8_f32 v3, v204, v205 op_sel:[0,0,1]
	v_lshlrev_b64 v[6:7], 8, v[6:7]
	v_lshl_add_u64 v[6:7], s[40:41], 0, v[6:7]
	v_permlane16_swap_b32_e32 v0, v2
	v_permlane16_swap_b32_e32 v1, v3
	v_lshl_add_u64 v[4:5], v[6:7], 0, v[4:5]
	global_store_dwordx4 v[4:5], v[0:3], off
	s_cbranch_vccnz .LBB0_1597
; #define PG8_BAR __builtin_amdgcn_s_barrier()
; template <class Sched> __device__ __forceinline__ unsigned gather_off(const Sched& S, int ui, int h, int i, int t, int KB) { asm volatile("" : "+v"(t)); int R, C; stage_rc(t * 16 + i * 8192, R, C); return (unsigned)(S.arow(ui, h * HALF + R) * KB + C * 2); }
;     ...
;         if constexpr (GATHER) {
; #pragma unroll
;             for (int h = 0; h < 2; ++h)
; #pragma unroll
;                 for (int i = 0; i < 2; ++i) oc[h][i] = gather_off(S, ui, h, i, tid, KB); }
;         if constexpr (ALIGN_EPI) { if (wr == 1) PG8_BAR; }
	s_nop 0
	v_mov_b32_e32 v0, v190
	v_mov_b32_e32 v13, 0x2000
	v_ashrrev_i32_e32 v2, 31, v0
	v_lshrrev_b32_e32 v2, 26, v2
	v_lshlrev_b32_e32 v1, 4, v0
	v_add_u32_e32 v2, v0, v2
	v_bfe_i32 v0, v0, 27, 1
	v_lshrrev_b32_e32 v0, 22, v0
	v_add_u32_e32 v0, v1, v0
	v_and_b32_e32 v0, 0xfffffc00, v0
	v_sub_u32_e32 v0, v1, v0
	v_lshrrev_b32_e32 v1, 4, v0
	v_bitop3_b32 v0, v1, v0, 32 bitop3:0x6c
	v_ashrrev_i32_e32 v1, 31, v0
	v_lshrrev_b32_e32 v1, 26, v1
	v_ashrrev_i32_e32 v2, 6, v2
	v_add_u32_e32 v1, v0, v1
	v_ashrrev_i32_e32 v4, 6, v1
	v_lshlrev_b32_e32 v3, 5, v2
	v_lshlrev_b32_e32 v2, 2, v4
	v_and_b32_e32 v4, 0xffffffc0, v3
	v_add3_u32 v2, s23, v2, v4
	v_mov_b32_e32 v4, v190
	ds_read_b32 v2, v2
	s_andn2_b64 vcc, exec, s[36:37]
	v_lshl_add_u32 v4, v4, 4, v13
	v_ashrrev_i32_e32 v5, 31, v4
	v_lshrrev_b32_e32 v5, 22, v5
	v_add_u32_e32 v5, v4, v5
	v_ashrrev_i32_e32 v6, 10, v5
	v_mul_i32_i24_e32 v5, 0x400, v6
	v_sub_u32_e32 v4, v4, v5
	v_lshrrev_b32_e32 v5, 4, v4
	v_bitop3_b32 v4, v5, v4, 32 bitop3:0x6c
	v_ashrrev_i32_e32 v5, 31, v4
	v_lshrrev_b32_e32 v5, 26, v5
	v_add_u32_e32 v5, v4, v5
	v_ashrrev_i32_e32 v8, 6, v5
	v_lshlrev_b32_e32 v7, 5, v6
	v_lshlrev_b32_e32 v6, 2, v8
	v_and_b32_e32 v8, 0xffffffc0, v7
	v_add3_u32 v6, s23, v6, v8
	v_mov_b32_e32 v8, v190
	ds_read_b32 v6, v6
	s_nop 0
	v_ashrrev_i32_e32 v10, 31, v8
	v_lshrrev_b32_e32 v10, 26, v10
	v_lshlrev_b32_e32 v9, 4, v8
	v_add_u32_e32 v10, v8, v10
	v_bfe_i32 v8, v8, 27, 1
	v_lshrrev_b32_e32 v8, 22, v8
	v_add_u32_e32 v8, v9, v8
	v_and_b32_e32 v8, 0xfffffc00, v8
	v_sub_u32_e32 v8, v9, v8
	v_lshrrev_b32_e32 v9, 4, v8
	v_bitop3_b32 v8, v9, v8, 32 bitop3:0x6c
	v_ashrrev_i32_e32 v9, 31, v8
	v_lshrrev_b32_e32 v9, 26, v9
	v_ashrrev_i32_e32 v10, 6, v10
	v_add_u32_e32 v9, v8, v9
	v_ashrrev_i32_e32 v12, 6, v9
	v_lshlrev_b32_e32 v11, 5, v10
	v_lshlrev_b32_e32 v10, 2, v12
	v_and_b32_e32 v12, 0xffffffc0, v11
	v_add3_u32 v10, s23, v10, v12
	v_mov_b32_e32 v12, v190
	ds_read_b32 v10, v10 offset:512
	s_nop 0
	v_lshl_add_u32 v12, v12, 4, v13
	v_ashrrev_i32_e32 v13, 31, v12
	v_lshrrev_b32_e32 v13, 22, v13
	v_add_u32_e32 v13, v12, v13
	v_ashrrev_i32_e32 v14, 10, v13
	v_mul_i32_i24_e32 v13, 0x400, v14
	v_sub_u32_e32 v12, v12, v13
	v_lshrrev_b32_e32 v13, 4, v12
	v_bitop3_b32 v12, v13, v12, 32 bitop3:0x6c
	v_ashrrev_i32_e32 v13, 31, v12
	v_lshrrev_b32_e32 v13, 26, v13
	v_add_u32_e32 v13, v12, v13
	v_ashrrev_i32_e32 v16, 6, v13
	v_lshlrev_b32_e32 v15, 5, v14
	v_lshlrev_b32_e32 v14, 2, v16
	v_and_b32_e32 v16, 0xffffffc0, v15
	v_add3_u32 v14, s23, v14, v16
	ds_read_b32 v14, v14 offset:512
	s_cbranch_vccnz .LBB0_1596
	s_barrier
	s_branch .LBB0_1596
